# RG-LRU sum-of-squares wave reduction: row_bcast steps as single v_add_f32_dpp instead of zero-init + v_mov_dpp + v_add (32 fewer VALU per chunk per wave)
# speedup vs baseline: 1.0019x; 1.0019x over previous
; #define LAS __attribute__((address_space(3)))
; #define MFMA16(a, b, c) __builtin_amdgcn_mfma_f32_16x16x32_bf16((a), (b), (c), 0, 0, 0)
; __device__ __forceinline__ float fsig(float x) { return __builtin_amdgcn_rcpf(1.0f + __builtin_amdgcn_exp2f(-LOG2E * x)); }
; __device__ __forceinline__ void unit(LAS unsigned char* lds, const bf16* __restrict__ xr, const bf16* __restrict__ yg, const float* __restrict__ conv_w, const float* __restrict__ conv_b, const bf16* __restrict__ wga_t, const bf16* __restrict__ wgx_t, ...
;     ...
;         {
;             f32x4 ar[2] = {}, ai[2] = {};
; #pragma unroll
;             for (int ks = 0; ks < 4; ++ks) { const bf16x8 xfr = *(const LAS bf16x8*)(lds + XA_OFF + (16 * tb + l15) * XA_P + 64 * ks + 16 * l4);
; #pragma unroll
;                 for (int dt = 0; dt < 2; ++dt) { ar[dt] = MFMA16(wf[0][dt][ks], xfr, ar[dt]); ai[dt] = MFMA16(wf[1][dt][ks], xfr, ai[dt]); } }
;             const int tk = 16 * tb + l15;
; #pragma unroll
;             for (int dt = 0; dt < 2; ++dt) { const int dl = dq * 32 + 16 * dt + 4 * l4; const f32x4 xo = *(const LAS f32x4*)(XF + tk * 64 + dl); f32x4 av, bv;
; #pragma unroll
;                 for (int r = 0; r < 4; ++r) { const float rg = fsig(ar[dt][r] + cba[dt][r]), ig = fsig(ai[dt][r] + cbx[dt][r]); const float la = rg * csp[dt][r];
;                     const float a_ = __builtin_amdgcn_exp2f(LOG2E * la); av[r] = a_;
;                     bv[r] = __builtin_amdgcn_sqrtf(fmaxf(1.0f - a_ * a_, 0.f)) * (ig * xo[r]); }
;                 *(LAS f32x4*)(SA + tk * 68 + dl) = av; *(LAS f32x4*)(SB + tk * 68 + dl) = bv; }
.LBB5_955:
	s_waitcnt lgkmcnt(0)
	s_barrier
	ds_read_b128 v[82:85], v161
	ds_read_b128 v[178:181], v161 offset:64
	ds_read_b128 v[214:217], v161 offset:128
	ds_read_b128 v[218:221], v161 offset:192
	s_and_b64 vcc, exec, s[4:5]
	s_waitcnt lgkmcnt(3)
	v_mfma_f32_16x16x32_bf16 v[86:89], v[2:5], v[82:85], 0
	v_mfma_f32_16x16x32_bf16 v[90:93], v[6:9], v[82:85], 0
	v_mfma_f32_16x16x32_bf16 v[94:97], v[34:37], v[82:85], 0
	v_mfma_f32_16x16x32_bf16 v[82:85], v[38:41], v[82:85], 0
	s_waitcnt lgkmcnt(2)
	v_mfma_f32_16x16x32_bf16 v[86:89], v[10:13], v[178:181], v[86:89]
	v_mfma_f32_16x16x32_bf16 v[90:93], v[14:17], v[178:181], v[90:93]
	v_mfma_f32_16x16x32_bf16 v[94:97], v[42:45], v[178:181], v[94:97]
	v_mfma_f32_16x16x32_bf16 v[82:85], v[46:49], v[178:181], v[82:85]
	s_waitcnt lgkmcnt(1)
	v_mfma_f32_16x16x32_bf16 v[86:89], v[18:21], v[214:217], v[86:89]
	v_mfma_f32_16x16x32_bf16 v[90:93], v[22:25], v[214:217], v[90:93]
	v_mfma_f32_16x16x32_bf16 v[182:185], v[50:53], v[214:217], v[94:97]
	v_mfma_f32_16x16x32_bf16 v[82:85], v[54:57], v[214:217], v[82:85]
	s_waitcnt lgkmcnt(0)
	v_mfma_f32_16x16x32_bf16 v[186:189], v[26:29], v[218:221], v[86:89]
	v_mfma_f32_16x16x32_bf16 v[94:97], v[30:33], v[218:221], v[90:93]
	s_nop 6
	v_add_f32_e32 v124, v66, v186
	v_mul_f32_e32 v124, 0xbfb8aa3b, v124
	v_exp_f32_e32 v124, v124
	v_mfma_f32_16x16x32_bf16 v[86:89], v[58:61], v[218:221], v[182:185]
	ds_read_b128 v[90:93], v152 offset:17408
	v_add_f32_e32 v94, v70, v94
	v_add_f32_e32 v96, v72, v96
	v_mfma_f32_16x16x32_bf16 v[82:85], v[62:65], v[218:221], v[82:85]
	v_add_f32_e32 v180, v68, v188
	v_mul_f32_e32 v180, 0xbfb8aa3b, v180
	v_exp_f32_e32 v180, v180
	v_mul_f32_e32 v94, 0xbfb8aa3b, v94
	v_mul_f32_e32 v96, 0xbfb8aa3b, v96
	v_add_f32_e32 v124, 1.0, v124
	v_exp_f32_e32 v94, v94
	v_add_f32_e32 v180, 1.0, v180
	v_exp_f32_e32 v96, v96
	v_rcp_f32_e32 v125, v124
	v_rcp_f32_e32 v181, v180
	v_add_f32_e32 v94, 1.0, v94
	v_add_f32_e32 v96, 1.0, v96
	v_rcp_f32_e32 v124, v94
	v_mul_f32_e32 v94, v139, v125
	v_rcp_f32_e32 v180, v96
	v_mul_f32_e32 v96, v141, v181
	v_mul_f32_e32 v94, 0x3fb8aa3b, v94
	v_mul_f32_e32 v96, 0x3fb8aa3b, v96
	v_exp_f32_e32 v94, v94
	v_exp_f32_e32 v96, v96
	v_add_f32_e32 v95, v71, v95
	v_add_f32_e32 v97, v73, v97
	v_fma_f32 v125, -v94, v94, 1.0
	v_fma_f32 v181, -v96, v96, 1.0
	v_max_f32_e32 v125, 0, v125
	v_max_f32_e32 v181, 0, v181
	v_sqrt_f32_e32 v178, v125
	v_add_f32_e32 v125, v67, v187
	v_sqrt_f32_e32 v182, v181
	v_add_f32_e32 v181, v69, v189
	v_mul_f32_e32 v125, 0xbfb8aa3b, v125
	v_mul_f32_e32 v181, 0xbfb8aa3b, v181
	v_exp_f32_e32 v125, v125
	v_exp_f32_e32 v181, v181
	v_mul_f32_e32 v95, 0xbfb8aa3b, v95
	v_mul_f32_e32 v97, 0xbfb8aa3b, v97
	v_add_f32_e32 v125, 1.0, v125
	v_exp_f32_e32 v95, v95
	v_add_f32_e32 v181, 1.0, v181
	v_exp_f32_e32 v97, v97
	v_rcp_f32_e32 v179, v125
	v_rcp_f32_e32 v183, v181
	v_add_f32_e32 v95, 1.0, v95
	v_add_f32_e32 v97, 1.0, v97
	v_rcp_f32_e32 v125, v95
	v_mul_f32_e32 v95, v140, v179
	v_rcp_f32_e32 v181, v97
	v_mul_f32_e32 v97, v142, v183
	v_mul_f32_e32 v95, 0x3fb8aa3b, v95
	v_mul_f32_e32 v97, 0x3fb8aa3b, v97
	v_exp_f32_e32 v95, v95
	v_exp_f32_e32 v97, v97
	v_add_f32_e32 v86, v74, v86
	v_add_f32_e32 v87, v75, v87
	v_add_f32_e32 v88, v76, v88
	v_add_f32_e32 v89, v77, v89
	v_fma_f32 v179, -v95, v95, 1.0
	v_fma_f32 v183, -v97, v97, 1.0
	v_mul_f32_e32 v86, 0xbfb8aa3b, v86
	v_mul_f32_e32 v87, 0xbfb8aa3b, v87
	v_mul_f32_e32 v88, 0xbfb8aa3b, v88
	v_mul_f32_e32 v89, 0xbfb8aa3b, v89
	v_max_f32_e32 v179, 0, v179
	v_max_f32_e32 v183, 0, v183
	v_exp_f32_e32 v86, v86
	v_exp_f32_e32 v87, v87
	v_exp_f32_e32 v88, v88
	v_exp_f32_e32 v89, v89
	v_sqrt_f32_e32 v179, v179
	v_sqrt_f32_e32 v183, v183
	v_add_f32_e32 v82, v78, v82
	v_add_f32_e32 v83, v79, v83
	v_add_f32_e32 v84, v80, v84
	v_add_f32_e32 v85, v81, v85
	v_mul_f32_e32 v82, 0xbfb8aa3b, v82
	v_mul_f32_e32 v83, 0xbfb8aa3b, v83
	v_mul_f32_e32 v84, 0xbfb8aa3b, v84
	v_mul_f32_e32 v85, 0xbfb8aa3b, v85
	s_waitcnt lgkmcnt(0)
	v_pk_mul_f32 v[90:91], v[90:91], v[124:125]
	v_pk_mul_f32 v[92:93], v[92:93], v[180:181]
	v_add_f32_e32 v86, 1.0, v86
	v_exp_f32_e32 v82, v82
	v_add_f32_e32 v87, 1.0, v87
	v_exp_f32_e32 v83, v83
	v_add_f32_e32 v88, 1.0, v88
	v_exp_f32_e32 v84, v84
	v_add_f32_e32 v89, 1.0, v89
	v_exp_f32_e32 v85, v85
	v_pk_mul_f32 v[92:93], v[92:93], v[182:183]
	v_pk_mul_f32 v[90:91], v[90:91], v[178:179]
	ds_write_b128 v153, v[94:97] offset:33792
	ds_write_b128 v153, v[90:93] offset:51200
	v_rcp_f32_e32 v94, v86
	v_rcp_f32_e32 v95, v87
	v_rcp_f32_e32 v96, v88
	v_rcp_f32_e32 v97, v89
	v_add_f32_e32 v82, 1.0, v82
	v_add_f32_e32 v83, 1.0, v83
	v_add_f32_e32 v84, 1.0, v84
	v_add_f32_e32 v85, 1.0, v85
	v_rcp_f32_e32 v86, v82
	v_mul_f32_e32 v82, v143, v94
	v_rcp_f32_e32 v87, v83
	v_mul_f32_e32 v83, v144, v95
	v_rcp_f32_e32 v88, v84
	v_mul_f32_e32 v84, v145, v96
	v_rcp_f32_e32 v89, v85
	v_mul_f32_e32 v85, v107, v97
	v_mul_f32_e32 v82, 0x3fb8aa3b, v82
	v_mul_f32_e32 v83, 0x3fb8aa3b, v83
	v_mul_f32_e32 v84, 0x3fb8aa3b, v84
	v_mul_f32_e32 v85, 0x3fb8aa3b, v85
	v_exp_f32_e32 v82, v82
	v_exp_f32_e32 v83, v83
	v_exp_f32_e32 v84, v84
	v_exp_f32_e32 v85, v85
	ds_read_b128 v[90:93], v152 offset:17472
	v_fma_f32 v94, -v82, v82, 1.0
	v_fma_f32 v95, -v83, v83, 1.0
	v_fma_f32 v96, -v84, v84, 1.0
	v_fma_f32 v97, -v85, v85, 1.0
	v_max_f32_e32 v94, 0, v94
	v_max_f32_e32 v95, 0, v95
	v_max_f32_e32 v96, 0, v96
	v_max_f32_e32 v97, 0, v97
	v_sqrt_f32_e32 v94, v94
	v_sqrt_f32_e32 v95, v95
	v_sqrt_f32_e32 v96, v96
	v_sqrt_f32_e32 v97, v97
	s_waitcnt lgkmcnt(0)
	v_pk_mul_f32 v[86:87], v[90:91], v[86:87]
	v_pk_mul_f32 v[88:89], v[92:93], v[88:89]
	v_pk_mul_f32 v[86:87], v[86:87], v[94:95]
	v_pk_mul_f32 v[88:89], v[88:89], v[96:97]
	ds_write_b128 v153, v[82:85] offset:33856
	ds_write_b128 v153, v[86:89] offset:51264
	s_waitcnt lgkmcnt(0)
	s_barrier
; __device__ __forceinline__ float bf2f(bf16 b) { return __uint_as_float(((unsigned)b) << 16); }
; __device__ __forceinline__ unsigned cvtpk(float lo, float hi) { const f32x2 v = {lo, hi}; return __builtin_bit_cast(unsigned, __builtin_convertvector(v, bf16x2_t)); }
; __device__ __forceinline__ void unit(LAS unsigned char* lds, const bf16* __restrict__ xr, const bf16* __restrict__ yg, const float* __restrict__ conv_w, const float* __restrict__ conv_b, const bf16* __restrict__ wga_t, const bf16* __restrict__ wgx_t, ...
;     ...
;         { float A = 1.f, B = 0.f;
; #pragma unroll
;             for (int i = 0; i < 8; ++i) { a8[i] = SA[(8 * sg + i) * 68 + cc]; b8[i] = SB[(8 * sg + i) * 68 + cc]; B = a8[i] * B + b8[i]; A *= a8[i]; }
;             SC[sg * 64 + cc] = (f32x2){A, B}; }
;         asm volatile("s_waitcnt lgkmcnt(0)" ::: "memory"); __builtin_amdgcn_s_barrier(); asm volatile("" ::: "memory");
;         {
;             float hcur = HS[cc];
; #pragma unroll
;             for (int s2 = 0; s2 < 7; ++s2) { const f32x2 ab = SC[s2 * 64 + cc]; if (s2 < sg) hcur = ab.x * hcur + ab.y; }
;             float ysq[8];
; #pragma unroll
;             for (int i = 0; i < 8; ++i) { hcur = a8[i] * hcur + b8[i]; const float x = bf2f(ycur[i]);
;                 const float u2 = 1.5957691216f * (x + 0.044715f * x * x * x);
;                 const float y = hcur * (x * __builtin_amdgcn_rcpf(1.0f + __builtin_amdgcn_exp2f(-LOG2E * u2))); outp[((size_t)t0 + i) * DM] = (bf16)(cvtpk(y, 0.f) & 0xffffu); ysq[i] = y * y; }
	v_add_u32_e32 v82, 0x8400, v156
	v_add_u32_e32 v83, 0xc800, v156
	ds_read2_b32 v[124:125], v82 offset1:68
	ds_read2_b32 v[96:97], v83 offset1:68
	ds_read2_b32 v[94:95], v82 offset0:136 offset1:204
	ds_read2_b32 v[92:93], v83 offset0:136 offset1:204
	v_add_u32_e32 v83, 0x8800, v156
	v_add_u32_e32 v178, 0xcc00, v156
	ds_read2_b32 v[88:89], v83 offset0:16 offset1:84
	ds_read2_b32 v[86:87], v178 offset0:16 offset1:84
	s_waitcnt lgkmcnt(4)
	v_fma_f32 v84, 0, v124, v96
	v_fma_f32 v84, v84, v125, v97
	s_waitcnt lgkmcnt(2)
	v_fma_f32 v82, v84, v94, v92
	v_fma_f32 v82, v82, v95, v93
	s_waitcnt lgkmcnt(0)
	v_fma_f32 v91, v82, v88, v86
	ds_read2_b32 v[84:85], v83 offset0:152 offset1:220
	ds_read2_b32 v[82:83], v178 offset0:152 offset1:220
	v_mul_f32_e32 v90, v124, v125
	v_mov_b32_e32 v178, v94
	v_mov_b32_e32 v179, v89
	v_mov_b32_e32 v180, v95
	v_mov_b32_e32 v181, v87
	v_mul_f32_e32 v182, v90, v94
	v_pk_fma_f32 v[90:91], v[90:91], v[178:179], v[180:181]
	v_mul_f32_e32 v182, v182, v95
	v_mov_b32_e32 v183, v91
	v_mov_b32_e32 v90, v88
	s_waitcnt lgkmcnt(1)
	v_mov_b32_e32 v91, v84
	v_pk_mul_f32 v[178:179], v[182:183], v[90:91]
	v_mov_b32_e32 v180, v89
	v_mov_b32_e32 v184, v89
	s_waitcnt lgkmcnt(0)
	v_mov_b32_e32 v185, v82
	v_pk_mul_f32 v[178:179], v[178:179], v[180:181]
	v_pk_fma_f32 v[90:91], v[182:183], v[90:91], v[184:185]
	v_mov_b32_e32 v180, v85
	v_mov_b32_e32 v90, v178
	v_pk_mul_f32 v[178:179], v[178:179], v[84:85]
	v_mov_b32_e32 v182, v85
	v_mov_b32_e32 v183, v83
	v_pk_mul_f32 v[178:179], v[178:179], v[180:181]
	v_pk_fma_f32 v[90:91], v[90:91], v[84:85], v[182:183]
	s_nop 0
	v_mov_b32_e32 v179, v91
	ds_write_b64 v149, v[178:179]
	s_waitcnt lgkmcnt(0)
	s_barrier
	ds_read_b32 v90, v131
	ds_read_b64 v[214:215], v129
	ds_read_b64 v[216:217], v129 offset:512
	ds_read_b64 v[218:219], v129 offset:1024
	ds_read_b64 v[220:221], v129 offset:1536
	ds_read_b64 v[222:223], v129 offset:2048
	ds_read_b64 v[224:225], v129 offset:2560
	ds_read_b64 v[226:227], v129 offset:3072
	s_waitcnt lgkmcnt(6)
	v_fmac_f32_e32 v215, v90, v214
	v_cndmask_b32_e64 v90, v215, v90, s[4:5]
	s_waitcnt lgkmcnt(5)
	v_fmac_f32_e32 v217, v90, v216
	v_cndmask_b32_e64 v90, v90, v217, s[50:51]
	s_waitcnt lgkmcnt(4)
	v_fmac_f32_e32 v219, v90, v218
	v_cndmask_b32_e64 v90, v90, v219, s[54:55]
	s_waitcnt lgkmcnt(3)
	v_fmac_f32_e32 v221, v90, v220
	v_cndmask_b32_e64 v90, v90, v221, s[60:61]
	s_waitcnt lgkmcnt(2)
	v_fmac_f32_e32 v223, v90, v222
	v_cndmask_b32_e64 v90, v90, v223, s[62:63]
	s_waitcnt lgkmcnt(1)
	v_fmac_f32_e32 v225, v90, v224
	v_cndmask_b32_e64 v90, v90, v225, s[64:65]
	s_waitcnt lgkmcnt(0)
	v_fmac_f32_e32 v227, v90, v226
	v_cndmask_b32_e64 v90, v90, v227, s[66:67]
	s_waitcnt lgkmcnt(0)
	v_fma_f32 v96, v124, v90, v96
	v_lshlrev_b32_e32 v90, 16, v177
	v_mul_f32_e32 v91, 0x3d372713, v90
	v_mul_f32_e32 v91, v91, v90
	v_fma_f32 v91, v91, v90, v90
	v_mul_f32_e32 v91, 0x3fcc422a, v91
	v_mul_f32_e32 v91, 0xbfb8aa3b, v91
	v_exp_f32_e32 v91, v91
	v_fmac_f32_e32 v97, v125, v96
	s_mov_b32 s70, 0x9c001000
	v_fma_f32 v92, v94, v97, v92
	v_add_f32_e32 v91, 1.0, v91
	v_rcp_f32_e32 v91, v91
	v_lshlrev_b32_e32 v94, 16, v171
	v_fmac_f32_e32 v93, v95, v92
	v_fma_f32 v86, v88, v93, v86
	v_mul_f32_e32 v90, v91, v90
	v_mul_f32_e32 v177, v90, v96
	v_lshl_add_u64 v[90:91], s[22:23], 0, v[122:123]
	v_add_co_u32_e32 v178, vcc, 0x9c000000, v90
	v_cvt_pk_bf16_f32 v124, v177, s0
	s_nop 0
	v_addc_co_u32_e32 v179, vcc, 0, v91, vcc
	v_lshlrev_b32_e32 v96, 16, v176
	global_store_short v[178:179], v124, off offset:2048
	v_mul_f32_e32 v124, 0x3d372713, v96
	v_mul_f32_e32 v124, v124, v96
	v_fma_f32 v124, v124, v96, v96
	v_mul_f32_e32 v124, 0x3fcc422a, v124
	v_mul_f32_e32 v124, 0xbfb8aa3b, v124
	v_exp_f32_e32 v124, v124
	v_lshlrev_b32_e32 v88, 16, v165
	v_fmac_f32_e32 v87, v89, v86
	v_fma_f32 v82, v84, v87, v82
	v_add_f32_e32 v124, 1.0, v124
	v_rcp_f32_e32 v124, v124
	v_lshlrev_b32_e32 v84, 16, v163
	v_fmac_f32_e32 v83, v85, v82
	v_mul_f32_e32 v178, v177, v177
	v_mul_f32_e32 v96, v124, v96
	v_mul_f32_e32 v176, v96, v97
	v_add_co_u32_e32 v124, vcc, s70, v90
	v_cvt_pk_bf16_f32 v96, v176, s0
	s_nop 0
	v_addc_co_u32_e32 v125, vcc, 0, v91, vcc
	global_store_short v[124:125], v96, off offset:2048
	v_mul_f32_e32 v96, 0x3d372713, v94
	v_mul_f32_e32 v96, v96, v94
	v_fma_f32 v96, v96, v94, v94
	v_mul_f32_e32 v96, 0x3fcc422a, v96
	v_mul_f32_e32 v96, 0xbfb8aa3b, v96
	v_exp_f32_e32 v96, v96
	s_mov_b32 s70, 0x9c002000
	v_mul_f32_e32 v124, v176, v176
	v_add_f32_e32 v96, 1.0, v96
	v_rcp_f32_e32 v96, v96
	s_nop 0
	v_mul_f32_e32 v94, v96, v94
	v_mul_f32_e32 v125, v94, v92
	v_add_co_u32_e32 v96, vcc, s70, v90
	v_cvt_pk_bf16_f32 v94, v125, s0
	s_nop 0
	v_addc_co_u32_e32 v97, vcc, 0, v91, vcc
	v_lshlrev_b32_e32 v92, 16, v166
	global_store_short v[96:97], v94, off offset:2048
	v_mul_f32_e32 v94, 0x3d372713, v92
	v_mul_f32_e32 v94, v94, v92
	v_fma_f32 v94, v94, v92, v92
	v_mul_f32_e32 v94, 0x3fcc422a, v94
	v_mul_f32_e32 v94, 0xbfb8aa3b, v94
	v_exp_f32_e32 v94, v94
	s_mov_b32 s70, 0x9c003000
	v_mul_f32_e32 v96, v125, v125
	v_add_f32_e32 v94, 1.0, v94
	v_rcp_f32_e32 v94, v94
	s_nop 0
	v_mul_f32_e32 v92, v94, v92
	v_mul_f32_e32 v97, v92, v93
	v_add_co_u32_e32 v94, vcc, s70, v90
	v_cvt_pk_bf16_f32 v92, v97, s0
	s_nop 0
	v_addc_co_u32_e32 v95, vcc, 0, v91, vcc
	global_store_short v[94:95], v92, off offset:2048
	v_mul_f32_e32 v92, 0x3d372713, v88
	v_mul_f32_e32 v92, v92, v88
	v_fma_f32 v92, v92, v88, v88
	v_mul_f32_e32 v92, 0x3fcc422a, v92
	v_mul_f32_e32 v92, 0xbfb8aa3b, v92
	v_exp_f32_e32 v92, v92
	s_mov_b32 s70, 0x9c004000
	v_mul_f32_e32 v94, v97, v97
	v_add_f32_e32 v92, 1.0, v92
	v_rcp_f32_e32 v92, v92
	s_nop 0
	v_mul_f32_e32 v88, v92, v88
; __device__ __forceinline__ float bf2f(bf16 b) { return __uint_as_float(((unsigned)b) << 16); }
; __device__ __forceinline__ unsigned cvtpk(float lo, float hi) { const f32x2 v = {lo, hi}; return __builtin_bit_cast(unsigned, __builtin_convertvector(v, bf16x2_t)); }
; __device__ __forceinline__ void unit(LAS unsigned char* lds, const bf16* __restrict__ xr, const bf16* __restrict__ yg, const float* __restrict__ conv_w, const float* __restrict__ conv_b, const bf16* __restrict__ wga_t, const bf16* __restrict__ wgx_t, ...
;     ...
;             for (int i = 0; i < 8; ++i) { hcur = a8[i] * hcur + b8[i]; const float x = bf2f(ycur[i]);
;                 const float u2 = 1.5957691216f * (x + 0.044715f * x * x * x);
;                 const float y = hcur * (x * __builtin_amdgcn_rcpf(1.0f + __builtin_amdgcn_exp2f(-LOG2E * u2))); outp[((size_t)t0 + i) * DM] = (bf16)(cvtpk(y, 0.f) & 0xffffu); ysq[i] = y * y; }
; #pragma unroll
;             for (int i = 0; i < 8; ++i) { float v = ysq[i];
;                 v += __builtin_bit_cast(float, __builtin_amdgcn_update_dpp(0, __builtin_bit_cast(int, v), 0xB1, 0xf, 0xf, true));
;                 v += __builtin_bit_cast(float, __builtin_amdgcn_update_dpp(0, __builtin_bit_cast(int, v), 0x4E, 0xf, 0xf, true));
;                 v += __builtin_bit_cast(float, __builtin_amdgcn_update_dpp(0, __builtin_bit_cast(int, v), 0x141, 0xf, 0xf, true));
;                 v += __builtin_bit_cast(float, __builtin_amdgcn_update_dpp(0, __builtin_bit_cast(int, v), 0x140, 0xf, 0xf, true));
;                 v += __builtin_bit_cast(float, __builtin_amdgcn_update_dpp(0, __builtin_bit_cast(int, v), 0x142, 0xa, 0xf, false));
;                 v += __builtin_bit_cast(float, __builtin_amdgcn_update_dpp(0, __builtin_bit_cast(int, v), 0x143, 0xc, 0xf, false));
;                 ysq[i] = v; }
;             if (lane == 63) {
; #pragma unroll
;                 for (int i = 0; i < 8; ++i) ssl[((size_t)b * SEQ + t0 + 8 * sg + i) * 16 + g] = ysq[i]; }
	v_mul_f32_e32 v95, v88, v86
	v_add_co_u32_e32 v92, vcc, s70, v90
	v_cvt_pk_bf16_f32 v88, v95, s0
	s_nop 0
	v_addc_co_u32_e32 v93, vcc, 0, v91, vcc
	v_lshlrev_b32_e32 v86, 16, v164
	global_store_short v[92:93], v88, off offset:2048
	v_mul_f32_e32 v88, 0x3d372713, v86
	v_mul_f32_e32 v88, v88, v86
	v_fma_f32 v88, v88, v86, v86
	v_mul_f32_e32 v88, 0x3fcc422a, v88
	v_mul_f32_e32 v88, 0xbfb8aa3b, v88
	v_exp_f32_e32 v88, v88
	s_mov_b32 s70, 0x9c005000
	v_mul_f32_e32 v92, v95, v95
	v_add_f32_e32 v88, 1.0, v88
	v_rcp_f32_e32 v88, v88
	s_nop 0
	v_mul_f32_e32 v86, v88, v86
	v_mul_f32_e32 v93, v86, v87
	v_add_co_u32_e32 v88, vcc, s70, v90
	v_cvt_pk_bf16_f32 v86, v93, s0
	s_nop 0
	v_addc_co_u32_e32 v89, vcc, 0, v91, vcc
	global_store_short v[88:89], v86, off offset:2048
	v_mul_f32_e32 v86, 0x3d372713, v84
	v_mul_f32_e32 v86, v86, v84
	v_fma_f32 v86, v86, v84, v84
	v_mul_f32_e32 v86, 0x3fcc422a, v86
	v_mul_f32_e32 v86, 0xbfb8aa3b, v86
	v_exp_f32_e32 v86, v86
	s_mov_b32 s70, 0x9c006000
	v_mul_f32_e32 v164, v93, v93
	v_mov_b32_dpp v89, v94 quad_perm:[1,0,3,2] row_mask:0xf bank_mask:0xf bound_ctrl:1
	v_add_f32_e32 v86, 1.0, v86
	v_rcp_f32_e32 v86, v86
	v_fmac_f32_e32 v89, v97, v97
	v_mov_b32_dpp v94, v164 quad_perm:[1,0,3,2] row_mask:0xf bank_mask:0xf bound_ctrl:1
	v_fmac_f32_e32 v94, v93, v93
	v_mul_f32_e32 v84, v86, v84
	v_mul_f32_e32 v163, v84, v82
	v_add_co_u32_e32 v86, vcc, s70, v90
	v_cvt_pk_bf16_f32 v84, v163, s0
	s_nop 0
	v_addc_co_u32_e32 v87, vcc, 0, v91, vcc
	v_lshlrev_b32_e32 v82, 16, v162
	global_store_short v[86:87], v84, off offset:2048
	v_mul_f32_e32 v84, 0x3d372713, v82
	v_mul_f32_e32 v84, v84, v82
	v_fma_f32 v84, v84, v82, v82
	v_mul_f32_e32 v84, 0x3fcc422a, v84
	v_mul_f32_e32 v84, 0xbfb8aa3b, v84
	v_exp_f32_e32 v84, v84
	s_mov_b32 s70, 0x9c007000
	v_mul_f32_e32 v165, v163, v163
	v_mov_b32_dpp v87, v96 quad_perm:[1,0,3,2] row_mask:0xf bank_mask:0xf bound_ctrl:1
	v_add_f32_e32 v84, 1.0, v84
	v_rcp_f32_e32 v84, v84
	v_fmac_f32_e32 v87, v125, v125
	v_add_f32_dpp v89, v89, v89 quad_perm:[2,3,0,1] row_mask:0xf bank_mask:0xf bound_ctrl:1
	v_add_f32_dpp v93, v94, v94 quad_perm:[2,3,0,1] row_mask:0xf bank_mask:0xf bound_ctrl:1
	v_mul_f32_e32 v82, v84, v82
	v_mul_f32_e32 v162, v82, v83
	v_add_co_u32_e32 v84, vcc, s70, v90
	v_cvt_pk_bf16_f32 v82, v162, s0
	s_nop 0
	v_addc_co_u32_e32 v85, vcc, 0, v91, vcc
	v_mul_f32_e32 v166, v162, v162
	v_mov_b32_dpp v91, v92 quad_perm:[1,0,3,2] row_mask:0xf bank_mask:0xf bound_ctrl:1
	global_store_short v[84:85], v82, off offset:2048
	v_mov_b32_dpp v82, v178 quad_perm:[1,0,3,2] row_mask:0xf bank_mask:0xf bound_ctrl:1
	v_mov_b32_dpp v85, v124 quad_perm:[1,0,3,2] row_mask:0xf bank_mask:0xf bound_ctrl:1
	v_fmac_f32_e32 v91, v95, v95
	v_mov_b32_dpp v95, v165 quad_perm:[1,0,3,2] row_mask:0xf bank_mask:0xf bound_ctrl:1
	v_mov_b32_dpp v97, v166 quad_perm:[1,0,3,2] row_mask:0xf bank_mask:0xf bound_ctrl:1
	v_fmac_f32_e32 v82, v177, v177
	v_fmac_f32_e32 v85, v176, v176
	v_fmac_f32_e32 v95, v163, v163
	v_fmac_f32_e32 v97, v162, v162
	v_add_f32_dpp v82, v82, v82 quad_perm:[2,3,0,1] row_mask:0xf bank_mask:0xf bound_ctrl:1
	v_add_f32_dpp v85, v85, v85 quad_perm:[2,3,0,1] row_mask:0xf bank_mask:0xf bound_ctrl:1
	v_add_f32_dpp v87, v87, v87 quad_perm:[2,3,0,1] row_mask:0xf bank_mask:0xf bound_ctrl:1
	v_add_f32_dpp v91, v91, v91 quad_perm:[2,3,0,1] row_mask:0xf bank_mask:0xf bound_ctrl:1
	v_add_f32_dpp v95, v95, v95 quad_perm:[2,3,0,1] row_mask:0xf bank_mask:0xf bound_ctrl:1
	v_add_f32_dpp v97, v97, v97 quad_perm:[2,3,0,1] row_mask:0xf bank_mask:0xf bound_ctrl:1
	v_add_f32_dpp v82, v82, v82 row_half_mirror row_mask:0xf bank_mask:0xf bound_ctrl:1
	v_add_f32_dpp v85, v85, v85 row_half_mirror row_mask:0xf bank_mask:0xf bound_ctrl:1
	v_add_f32_dpp v87, v87, v87 row_half_mirror row_mask:0xf bank_mask:0xf bound_ctrl:1
	v_add_f32_dpp v89, v89, v89 row_half_mirror row_mask:0xf bank_mask:0xf bound_ctrl:1
	v_add_f32_dpp v91, v91, v91 row_half_mirror row_mask:0xf bank_mask:0xf bound_ctrl:1
	v_add_f32_dpp v93, v93, v93 row_half_mirror row_mask:0xf bank_mask:0xf bound_ctrl:1
	v_add_f32_dpp v95, v95, v95 row_half_mirror row_mask:0xf bank_mask:0xf bound_ctrl:1
	v_add_f32_dpp v97, v97, v97 row_half_mirror row_mask:0xf bank_mask:0xf bound_ctrl:1
	v_add_f32_dpp v82, v82, v82 row_mirror row_mask:0xf bank_mask:0xf bound_ctrl:1
	v_add_f32_dpp v85, v85, v85 row_mirror row_mask:0xf bank_mask:0xf bound_ctrl:1
	v_add_f32_dpp v87, v87, v87 row_mirror row_mask:0xf bank_mask:0xf bound_ctrl:1
	v_add_f32_dpp v89, v89, v89 row_mirror row_mask:0xf bank_mask:0xf bound_ctrl:1
	v_add_f32_dpp v91, v91, v91 row_mirror row_mask:0xf bank_mask:0xf bound_ctrl:1
	v_add_f32_dpp v93, v93, v93 row_mirror row_mask:0xf bank_mask:0xf bound_ctrl:1
	v_add_f32_dpp v95, v95, v95 row_mirror row_mask:0xf bank_mask:0xf bound_ctrl:1
	v_add_f32_dpp v97, v97, v97 row_mirror row_mask:0xf bank_mask:0xf bound_ctrl:1
	v_add_f32_dpp v82, v82, v82 row_bcast:15 row_mask:0xa bank_mask:0xf
	v_add_f32_dpp v85, v85, v85 row_bcast:15 row_mask:0xa bank_mask:0xf
	v_add_f32_dpp v87, v87, v87 row_bcast:15 row_mask:0xa bank_mask:0xf
	v_add_f32_dpp v89, v89, v89 row_bcast:15 row_mask:0xa bank_mask:0xf
	v_add_f32_dpp v91, v91, v91 row_bcast:15 row_mask:0xa bank_mask:0xf
	v_add_f32_dpp v93, v93, v93 row_bcast:15 row_mask:0xa bank_mask:0xf
	v_add_f32_dpp v95, v95, v95 row_bcast:15 row_mask:0xa bank_mask:0xf
	v_add_f32_dpp v97, v97, v97 row_bcast:15 row_mask:0xa bank_mask:0xf
	v_add_f32_dpp v82, v82, v82 row_bcast:31 row_mask:0xc bank_mask:0xf
	v_add_f32_dpp v85, v85, v85 row_bcast:31 row_mask:0xc bank_mask:0xf
	v_add_f32_dpp v87, v87, v87 row_bcast:31 row_mask:0xc bank_mask:0xf
	v_add_f32_dpp v89, v89, v89 row_bcast:31 row_mask:0xc bank_mask:0xf
	v_add_f32_dpp v91, v91, v91 row_bcast:31 row_mask:0xc bank_mask:0xf
	v_add_f32_dpp v93, v93, v93 row_bcast:31 row_mask:0xc bank_mask:0xf
	v_add_f32_dpp v95, v95, v95 row_bcast:31 row_mask:0xc bank_mask:0xf
	v_add_f32_dpp v97, v97, v97 row_bcast:31 row_mask:0xc bank_mask:0xf
	s_and_saveexec_b64 s[70:71], s[8:9]
	s_cbranch_execz .LBB5_965
	s_add_u32 s92, s22, s34
	s_addc_u32 s93, s23, s89
	global_store_dword v99, v82, s[92:93] offset:-256
	global_store_dword v99, v85, s[92:93] offset:-192
	global_store_dword v99, v87, s[92:93] offset:-128
	global_store_dword v99, v89, s[92:93] offset:-64
	global_store_dword v99, v91, s[92:93]
	global_store_dword v99, v93, s[92:93] offset:64
	global_store_dword v99, v95, s[92:93] offset:128
	global_store_dword v99, v97, s[92:93] offset:192
